# v028 + attention unit header no longer drains the previous unit's output stores before issuing the next Q loads
# baseline (speedup 1.0000x reference)
.LBB0_1410:
	s_ashr_i32 s2, s71, 8
	s_lshl_b32 s1, s71, 8
	s_lshl_b32 s0, s2, 12
	s_and_b32 s1, s1, 0xf00
	s_bfe_u32 s72, s71, 0x40004
	s_or_b32 s34, s0, s1
	s_lshl_b32 s66, s72, 9
	s_ashr_i32 s35, s34, 31
	s_mul_i32 s1, s34, 0x1800
	s_mul_hi_i32 s0, s34, 0x1800
	s_add_u32 s1, s25, s1
	s_addc_u32 s3, s38, s0
	s_mul_i32 s0, s72, 0x180
	v_mov_b32_e32 v12, v0
	s_add_u32 s0, s1, s0
	s_addc_u32 s1, s3, 0
	v_ashrrev_i32_e32 v13, 6, v12
	v_and_b32_e32 v155, 31, v12
	v_lshlrev_b32_e32 v158, 5, v13
	s_waitcnt lgkmcnt(0)
	v_bfe_u32 v176, v12, 5, 1
	v_or_b32_e32 v4, v158, v155
	v_mov_b64_e32 v[2:3], s[0:1]
	v_mad_i64_i32 v[2:3], s[0:1], v4, s45, v[2:3]
	v_lshlrev_b32_e32 v156, 4, v176
	v_lshl_add_u64 v[10:11], v[2:3], 0, v[156:157]
	global_load_dwordx4 v[2:5], v[10:11], off offset:320
	global_load_dwordx4 v[6:9], v[10:11], off offset:352
	global_load_dwordx4 v[134:137], v[10:11], off
	global_load_dwordx4 v[130:133], v[10:11], off offset:32
	global_load_dwordx4 v[126:129], v[10:11], off offset:64
	global_load_dwordx4 v[122:125], v[10:11], off offset:96
	global_load_dwordx4 v[118:121], v[10:11], off offset:128
	global_load_dwordx4 v[114:117], v[10:11], off offset:160
	global_load_dwordx4 v[110:113], v[10:11], off offset:192
	global_load_dwordx4 v[106:109], v[10:11], off offset:224
	global_load_dwordx4 v[102:105], v[10:11], off offset:256
	global_load_dwordx4 v[98:101], v[10:11], off offset:288
	s_mulk_i32 s2, 0x1100
	s_ashr_i32 s3, s2, 31
	s_lshl_b64 s[0:1], s[2:3], 13
	s_add_u32 s4, s39, s0
	s_addc_u32 s5, s40, s1
	s_add_u32 s36, s4, s66
	s_addc_u32 s37, s5, 0
	s_lshl_b64 s[4:5], s[2:3], 7
	v_lshlrev_b32_e32 v59, 3, v12
	v_readfirstlane_b32 s67, v13
	s_add_u32 s2, s41, s4
	v_and_b32_e32 v52, 63, v12
	v_mul_lo_u32 v16, v13, s45
	v_and_b32_e32 v13, 24, v59
	s_addc_u32 s3, s42, s5
	s_lshl_b32 s33, s67, 3
	s_lshl_b32 s64, s67, 2
	v_lshlrev_b32_e32 v64, 4, v52
	v_add_u32_e32 v16, s47, v16
	v_and_or_b32 v56, v12, 32, v13
	v_lshl_or_b32 v13, s67, 6, v52
	s_and_b32 s73, s33, -16
	s_and_b32 s74, s64, 4
	v_bfe_u32 v15, v12, 4, 2
	v_lshrrev_b32_e32 v14, 1, v12
	v_add_u32_e32 v180, v16, v64
	v_lshlrev_b32_e32 v16, 3, v13
	v_lshrrev_b32_e32 v13, 4, v13
	s_cmp_lg_u32 0, -1
	v_and_b32_e32 v54, 8, v14
	v_lshlrev_b32_e32 v14, 12, v15
	v_xor_b32_e32 v13, v13, v12
	v_or3_b32 v11, v15, s33, 4
	s_cselect_b32 s75, 0, 0
	s_lshl_b32 s33, s67, 11
	v_and_b32_e32 v17, 15, v12
	v_bitop3_b32 v18, v15, v12, 15 bitop3:0x78
	v_lshrrev_b32_e32 v19, 3, v12
	v_and_b32_e32 v19, 8, v19
	v_xor_b32_e32 v18, v18, v19
	v_lshl_or_b32 v55, s67, 15, v14
	v_lshlrev_b32_e32 v13, 3, v13
	s_cmp_lg_u32 s49, -1
	v_bfe_u32 v53, v12, 2, 2
	v_lshl_or_b32 v14, v18, 3, v55
	v_and_b32_e32 v57, 56, v13
	v_bitop3_b32 v13, v11, v17, 15 bitop3:0x6c
	s_cselect_b32 s64, s49, 0
	v_mov_b32_e32 v15, v157
	v_or3_b32 v10, v54, v53, s73
	v_lshlrev_b32_e32 v58, 3, v13
	s_add_i32 s76, s33, s64
	s_add_i32 s64, s33, s75
	s_lshl_b32 s65, s67, 10
	v_lshlrev_b64 v[50:51], 1, v[14:15]
	v_or_b32_e32 v10, s74, v10
	v_lshl_or_b32 v18, v11, 12, v58
	s_cmp_lg_u32 s50, -1
	s_mov_b32 m0, s76
	v_mov_b32_e32 v19, v157
	v_lshl_or_b32 v10, v10, 12, v56
	s_cselect_b32 s77, s50, 0
	v_mov_b32_e32 v11, v157
	v_and_or_b32 v16, v16, s48, v57
	s_add_i32 s77, s65, s77
	s_waitcnt vmcnt(11)
	ds_write_b128 v180, v[2:5]
	s_waitcnt vmcnt(10)
	ds_write_b128 v180, v[6:9] offset:1024
	v_lshl_add_u64 v[2:3], s[36:37], 0, v[50:51]
	global_load_lds_dwordx4 v[2:3], off
	v_lshlrev_b64 v[2:3], 1, v[18:19]
	v_lshl_add_u64 v[4:5], s[36:37], 0, v[2:3]
	s_add_i32 m0, s76, 0x400
	v_mov_b32_e32 v17, v157
	v_lshlrev_b64 v[6:7], 1, v[10:11]
	global_load_lds_dwordx4 v[4:5], off
	v_lshl_add_u64 v[4:5], v[16:17], 1, s[2:3]
	s_mov_b32 m0, s77
	v_lshl_add_u64 v[8:9], s[36:37], 0, v[6:7]
	s_mov_b64 s[2:3], 0x100
	v_or_b32_e32 v20, 64, v10
	global_load_lds_dwordx4 v[4:5], off
	v_lshl_add_u64 v[10:11], v[8:9], 0, s[2:3]
	s_mov_b32 m0, s64
	s_mov_b64 s[2:3], 0x180
	global_load_lds_dwordx4 v[10:11], off
	s_add_i32 m0, s64, 0x400
	v_lshl_add_u64 v[8:9], v[8:9], 0, s[2:3]
	s_add_u32 s2, s36, 0x80000
	s_addc_u32 s3, s37, 0
	global_load_lds_dwordx4 v[8:9], off
	v_lshl_add_u64 v[8:9], s[2:3], 0, v[50:51]
	s_add_i32 m0, s76, 0x4000
	v_lshl_add_u64 v[2:3], s[2:3], 0, v[2:3]
	global_load_lds_dwordx4 v[8:9], off
	s_add_i32 m0, s76, 0x4400
	s_mov_b64 s[2:3], 0x2000
	global_load_lds_dwordx4 v[2:3], off
	s_add_i32 m0, s77, 0x2000
	v_lshl_add_u64 v[2:3], v[4:5], 0, s[2:3]
	s_add_u32 s2, s36, 0x80100
	s_addc_u32 s3, s37, 0
	v_mov_b32_e32 v21, v157
	global_load_lds_dwordx4 v[2:3], off
	v_lshl_add_u64 v[2:3], s[2:3], 0, v[6:7]
	s_add_i32 m0, s64, 0x4000
	v_lshlrev_b32_e32 v10, 8, v155
	global_load_lds_dwordx4 v[2:3], off
	v_lshl_add_u64 v[2:3], v[20:21], 1, s[2:3]
	s_add_i32 m0, s64, 0x4400
	v_or_b32_e32 v13, 32, v156
	global_load_lds_dwordx4 v[2:3], off
	v_lshlrev_b32_e32 v2, 4, v12
	v_and_b32_e32 v11, 0xf0, v2
	v_bitop3_b32 v182, v156, v10, v11 bitop3:0xde
	v_add_u32_e32 v183, 0, v182
	s_waitcnt vmcnt(0)
	s_waitcnt vmcnt(0) lgkmcnt(0)
	s_barrier
	ds_read_b128 v[2:5], v183 offset:49152
	ds_read_b128 v[6:9], v183 offset:57344
	s_waitcnt lgkmcnt(1)
	v_mfma_f32_32x32x16_bf16 v[34:49], v[2:5], v[134:137], 0
	v_bitop3_b32 v184, v13, v10, v11 bitop3:0xde
	v_add_u32_e32 v185, 0, v184
	v_or_b32_e32 v14, 64, v156
	v_bitop3_b32 v186, v14, v10, v11 bitop3:0xde
	v_add_u32_e32 v187, 0, v186
	v_or_b32_e32 v65, 0x60, v156
	v_bitop3_b32 v188, v65, v10, v11 bitop3:0xde
	s_waitcnt lgkmcnt(0)
	v_mfma_f32_32x32x16_bf16 v[18:33], v[6:9], v[134:137], 0
	ds_read_b128 v[2:5], v185 offset:49152
	ds_read_b128 v[6:9], v185 offset:57344
	v_add_u32_e32 v189, 0, v188
	v_cmp_gt_u32_e64 s[2:3], 32, v52
	s_mov_b32 s36, -1
	s_mov_b32 s37, 0
	v_mov_b32_e32 v178, 0
	s_waitcnt lgkmcnt(1)
	v_mfma_f32_32x32x16_bf16 v[34:49], v[2:5], v[130:133], v[34:49]
	s_waitcnt lgkmcnt(0)
	v_mfma_f32_32x32x16_bf16 v[18:33], v[6:9], v[130:133], v[18:33]
	ds_read_b128 v[2:5], v187 offset:49152
	ds_read_b128 v[6:9], v187 offset:57344
	s_waitcnt lgkmcnt(1)
	v_mfma_f32_32x32x16_bf16 v[34:49], v[2:5], v[126:129], v[34:49]
	s_waitcnt lgkmcnt(0)
	v_mfma_f32_32x32x16_bf16 v[18:33], v[6:9], v[126:129], v[18:33]
	ds_read_b128 v[2:5], v189 offset:49152
	ds_read_b128 v[6:9], v189 offset:57344
	s_waitcnt lgkmcnt(1)
	v_mfma_f32_32x32x16_bf16 v[34:49], v[2:5], v[122:125], v[34:49]
	v_or_b32_e32 v2, 0x80, v156
	v_bitop3_b32 v190, v2, v10, v11 bitop3:0xde
	v_add_u32_e32 v191, 0, v190
	s_waitcnt lgkmcnt(0)
	v_mfma_f32_32x32x16_bf16 v[18:33], v[6:9], v[122:125], v[18:33]
	ds_read_b128 v[2:5], v191 offset:49152
	ds_read_b128 v[6:9], v191 offset:57344
	s_waitcnt lgkmcnt(1)
	v_mfma_f32_32x32x16_bf16 v[34:49], v[2:5], v[118:121], v[34:49]
	v_or_b32_e32 v2, 0xa0, v156
	v_bitop3_b32 v192, v2, v10, v11 bitop3:0xde
	v_add_u32_e32 v193, 0, v192
	s_waitcnt lgkmcnt(0)
	v_mfma_f32_32x32x16_bf16 v[18:33], v[6:9], v[118:121], v[18:33]
	ds_read_b128 v[2:5], v193 offset:49152
	ds_read_b128 v[6:9], v193 offset:57344
	s_waitcnt lgkmcnt(1)
	v_mfma_f32_32x32x16_bf16 v[34:49], v[2:5], v[114:117], v[34:49]
	v_or_b32_e32 v2, 0xc0, v156
	v_bitop3_b32 v194, v2, v10, v11 bitop3:0xde
	v_add_u32_e32 v195, 0, v194
	s_waitcnt lgkmcnt(0)
	v_mfma_f32_32x32x16_bf16 v[18:33], v[6:9], v[114:117], v[18:33]
	ds_read_b128 v[2:5], v195 offset:49152
	ds_read_b128 v[6:9], v195 offset:57344
	s_waitcnt lgkmcnt(1)
	v_mfma_f32_32x32x16_bf16 v[34:49], v[2:5], v[110:113], v[34:49]
	v_or_b32_e32 v2, 0xe0, v156
	v_bitop3_b32 v196, v2, v10, v11 bitop3:0xde
	v_add_u32_e32 v197, 0, v196
	v_lshlrev_b32_e32 v10, 7, v155
	v_and_b32_e32 v11, 0x70, v59
	v_bitop3_b32 v199, v156, v10, v11 bitop3:0xde
	v_add_u32_e32 v200, s50, v199
	s_waitcnt lgkmcnt(0)
	v_mfma_f32_32x32x16_bf16 v[18:33], v[6:9], v[110:113], v[18:33]
	ds_read_b128 v[2:5], v197 offset:49152
	ds_read_b128 v[6:9], v197 offset:57344
	v_bitop3_b32 v201, v13, v10, v11 bitop3:0xde
	v_add_u32_e32 v202, s50, v201
	v_bitop3_b32 v203, v14, v10, v11 bitop3:0xde
	v_add_u32_e32 v204, s50, v203
	v_bitop3_b32 v205, v65, v10, v11 bitop3:0xde
	v_add_u32_e32 v206, s50, v205
	s_waitcnt lgkmcnt(1)
	v_mfma_f32_32x32x16_bf16 v[34:49], v[2:5], v[106:109], v[34:49]
	v_lshlrev_b32_e32 v59, 3, v52
	s_waitcnt lgkmcnt(0)
	v_mfma_f32_32x32x16_bf16 v[18:33], v[6:9], v[106:109], v[18:33]
	ds_read_b128 v[2:5], v200
	ds_read_b128 v[6:9], v200 offset:4096
	s_waitcnt lgkmcnt(1)
	v_mfma_f32_32x32x16_bf16 v[34:49], v[2:5], v[102:105], v[34:49]
	s_waitcnt lgkmcnt(0)
	v_mfma_f32_32x32x16_bf16 v[18:33], v[6:9], v[102:105], v[18:33]
	ds_read_b128 v[2:5], v202
	ds_read_b128 v[6:9], v202 offset:4096
	s_waitcnt lgkmcnt(1)
	v_mfma_f32_32x32x16_bf16 v[34:49], v[2:5], v[98:101], v[34:49]
	s_waitcnt lgkmcnt(0)
	v_mfma_f32_32x32x16_bf16 v[18:33], v[6:9], v[98:101], v[18:33]
	ds_read_b128 v[2:5], v204
	ds_read_b128 v[6:9], v180
	ds_read_b128 v[14:17], v204 offset:4096
	ds_read_b128 v[60:63], v180 offset:1024
	s_waitcnt lgkmcnt(2)
	v_mfma_f32_32x32x16_bf16 v[34:49], v[2:5], v[6:9], v[34:49]
	ds_read_b128 v[2:5], v206
	s_waitcnt lgkmcnt(2)
	v_mfma_f32_32x32x16_bf16 v[18:33], v[14:17], v[6:9], v[18:33]
	v_and_b32_e32 v6, 0x3fffffc0, v12
	v_lshl_add_u32 v159, v6, 2, s46
	v_and_b32_e32 v6, 0xc0, v64
	ds_read_b128 v[64:67], v206 offset:4096
	v_lshl_add_u32 v177, v155, 2, v159
	s_waitcnt lgkmcnt(0)
	s_barrier
	v_mfma_f32_32x32x16_bf16 v[34:49], v[2:5], v[60:63], v[34:49]
	v_lshlrev_b32_e32 v3, 1, v12
	v_and_or_b32 v2, v59, 24, v6
	v_and_b32_e32 v3, 32, v3
	v_and_b32_e32 v4, 0x100, v59
	v_or3_b32 v179, v2, v3, v4
	v_mov_b64_e32 v[2:3], s[8:9]
	v_mov_b64_e32 v[16:17], s[22:23]
	v_mfma_f32_32x32x16_bf16 v[18:33], v[64:67], v[60:63], v[18:33]
	s_nop 3
	v_max_f32_e32 v60, v35, v35
	v_max_f32_e32 v61, v34, v34
	v_max_f32_e32 v60, v61, v60
	v_max3_f32 v60, v60, v36, v37
	v_max3_f32 v60, v60, v38, v39
	v_max3_f32 v60, v60, v40, v41
	v_max3_f32 v60, v60, v42, v43
	v_max3_f32 v60, v60, v44, v45
	v_max3_f32 v60, v60, v46, v47
	v_max3_f32 v60, v60, v48, v49
	v_max3_f32 v60, v60, v18, v19
	v_max3_f32 v60, v60, v20, v21
	v_max3_f32 v60, v60, v22, v23
	v_max3_f32 v60, v60, v24, v25
	v_max3_f32 v60, v60, v26, v27
	v_max3_f32 v60, v60, v28, v29
	v_max3_f32 v60, v60, v30, v31
	v_max3_f32 v60, v60, v32, v33
	v_mov_b32_e32 v61, v60
	s_nop 1
	v_permlane32_swap_b32_e32 v60, v61
	v_max_f32_e32 v61, v61, v61
	v_max_f32_e32 v60, v60, v60
	v_max_f32_e32 v60, v60, v61
	v_add_f32_e32 v61, 0x7149f2ca, v60
	v_max_f32_e32 v60, 0xf149f2ca, v60
	v_cmp_ge_f32_e32 vcc, s51, v61
	v_sub_f32_e32 v61, 0xf149f2ca, v60
	v_mul_f32_e32 v61, 0x3dd53b94, v61
	v_exp_f32_e32 v61, v61
	s_cmp_eq_u64 vcc, exec
	s_cselect_b64 vcc, -1, 0
	v_cndmask_b32_e32 v208, v60, v1, vcc
	v_mul_f32_e32 v60, 0xbdd53b94, v208
	v_cndmask_b32_e64 v207, v61, 1.0, vcc
	v_mov_b32_e32 v61, v60
	v_fmac_f32_e32 v61, 0x3dd53b94, v49
	v_pk_fma_f32 v[152:153], v[18:19], s[24:25], v[60:61] op_sel_hi:[1,0,0]
	v_lshl_or_b32 v18, s67, 9, v59
	v_and_or_b32 v18, v18, s48, v57
	v_mov_b32_e32 v19, v157
	v_lshl_add_u64 v[160:161], v[18:19], 1, s[4:5]
	v_or_b32_e32 v18, s73, v54
	v_fmamk_f32 v34, v34, 0x3dd53b94, v60
	v_fmamk_f32 v35, v35, 0x3dd53b94, v60
	v_fmamk_f32 v36, v36, 0x3dd53b94, v60
	v_fmamk_f32 v37, v37, 0x3dd53b94, v60
	v_fmamk_f32 v38, v38, 0x3dd53b94, v60
	v_fmamk_f32 v39, v39, 0x3dd53b94, v60
	v_fmamk_f32 v40, v40, 0x3dd53b94, v60
	v_fmamk_f32 v41, v41, 0x3dd53b94, v60
	v_fmamk_f32 v42, v42, 0x3dd53b94, v60
	v_fmamk_f32 v43, v43, 0x3dd53b94, v60
	v_fmamk_f32 v44, v44, 0x3dd53b94, v60
	v_fmamk_f32 v45, v45, 0x3dd53b94, v60
	v_fmamk_f32 v46, v46, 0x3dd53b94, v60
	v_fmamk_f32 v47, v47, 0x3dd53b94, v60
	v_fmamk_f32 v48, v48, 0x3dd53b94, v60
	v_or3_b32 v18, v18, s74, v53
	v_exp_f32_e32 v239, v34
	v_exp_f32_e32 v241, v35
	v_exp_f32_e32 v237, v36
	v_exp_f32_e32 v240, v37
	v_exp_f32_e32 v236, v38
	v_exp_f32_e32 v238, v39
	v_exp_f32_e32 v234, v40
	v_exp_f32_e32 v235, v41
	v_exp_f32_e32 v231, v42
	v_exp_f32_e32 v233, v43
	v_exp_f32_e32 v230, v44
	v_exp_f32_e32 v232, v45
	v_exp_f32_e32 v227, v46
	v_exp_f32_e32 v229, v47
	v_exp_f32_e32 v226, v48
	v_exp_f32_e32 v228, v61
	s_or_b32 s0, s0, s66
	v_lshl_or_b32 v18, v18, 12, v56
	s_movk_i32 s4, 0x4000
	v_lshl_add_u64 v[162:163], v[18:19], 1, s[0:1]
	v_or3_b32 v18, v55, v58, s4
	v_mov_b64_e32 v[4:5], s[10:11]
	v_mov_b64_e32 v[6:7], s[12:13]
	v_mov_b64_e32 v[8:9], s[14:15]
	v_mov_b64_e32 v[10:11], s[16:17]
	v_mov_b64_e32 v[12:13], s[18:19]
	v_mov_b64_e32 v[14:15], s[20:21]
	v_pk_fma_f32 v[138:139], v[32:33], s[24:25], v[60:61] op_sel_hi:[1,0,0]
	v_pk_fma_f32 v[140:141], v[30:31], s[24:25], v[60:61] op_sel_hi:[1,0,0]
	v_pk_fma_f32 v[142:143], v[28:29], s[24:25], v[60:61] op_sel_hi:[1,0,0]
	v_pk_fma_f32 v[144:145], v[26:27], s[24:25], v[60:61] op_sel_hi:[1,0,0]
	v_pk_fma_f32 v[146:147], v[24:25], s[24:25], v[60:61] op_sel_hi:[1,0,0]
	v_pk_fma_f32 v[148:149], v[22:23], s[24:25], v[60:61] op_sel_hi:[1,0,0]
	v_pk_fma_f32 v[150:151], v[20:21], s[24:25], v[60:61] op_sel_hi:[1,0,0]
	v_lshl_add_u64 v[164:165], s[0:1], 0, v[50:51]
	v_lshl_add_u64 v[166:167], v[18:19], 1, s[0:1]
	v_mov_b64_e32 v[64:65], v[16:17]
	v_mov_b64_e32 v[48:49], v[16:17]
	v_mov_b64_e32 v[32:33], v[16:17]
	v_add_u32_e32 v181, s75, v179
	v_mov_b64_e32 v[62:63], v[14:15]
	v_mov_b64_e32 v[60:61], v[12:13]
	v_mov_b64_e32 v[58:59], v[10:11]
	v_mov_b64_e32 v[56:57], v[8:9]
	v_mov_b64_e32 v[54:55], v[6:7]
	v_mov_b64_e32 v[52:53], v[4:5]
	v_mov_b64_e32 v[50:51], v[2:3]
	v_mov_b64_e32 v[46:47], v[14:15]
	v_mov_b64_e32 v[44:45], v[12:13]
	v_mov_b64_e32 v[42:43], v[10:11]
	v_mov_b64_e32 v[40:41], v[8:9]
	v_mov_b64_e32 v[38:39], v[6:7]
	v_mov_b64_e32 v[36:37], v[4:5]
	v_mov_b64_e32 v[34:35], v[2:3]
	v_mov_b64_e32 v[30:31], v[14:15]
	v_mov_b64_e32 v[28:29], v[12:13]
	v_mov_b64_e32 v[26:27], v[10:11]
	v_mov_b64_e32 v[24:25], v[8:9]
	v_mov_b64_e32 v[22:23], v[6:7]
	v_mov_b64_e32 v[20:21], v[4:5]
	v_mov_b64_e32 v[18:19], v[2:3]
	s_mov_b32 s66, 2
